# stack + SWA Q/sink prefetch one iteration ahead + accumulator clears interleaved into the SwiGLU fp8 epilogue
# baseline (speedup 1.0000x reference)
.LBB0_1732:
	s_ashr_i32 s49, s48, 31
	s_lshl_b64 s[0:1], s[48:49], 8
	s_add_u32 s0, s0, s82
	s_addc_u32 s1, s1, s92
	s_mulk_i32 s1, 0xe00
	s_mul_hi_u32 s16, s0, 0xe00
	s_add_i32 s16, s16, s1
	s_mulk_i32 s0, 0xe00
	s_add_u32 s0, s80, s0
	s_addc_u32 s1, s81, s16
	s_lshl_b32 s16, s46, 7
	s_ashr_i32 s17, s16, 31
	s_add_u32 s0, s0, s16
	s_addc_u32 s1, s1, s17
	s_add_u32 s0, s0, s83
	s_addc_u32 s1, s1, 0
	s_movk_i32 s16, 0xe00
	v_mov_b32_e32 v130, v164
	v_mov_b32_e32 v131, v165
	v_mov_b32_e32 v136, 0
	v_mov_b32_e32 v137, 0
	v_mov_b32_e32 v138, 0
	v_mov_b32_e32 v139, 0
	v_mul_lo_u32 v130, v130, s16
	v_lshl_add_u32 v202, v131, 3, v130
	v_pk_mul_f32 v[98:99], v[114:115], v[98:99]
	v_pk_mul_f32 v[100:101], v[116:117], v[100:101]
	v_pk_mul_f32 v[102:103], v[118:119], v[102:103]
	v_pk_mul_f32 v[104:105], v[120:121], v[104:105]
	v_exp_f32_e32 v114, v114
	v_exp_f32_e32 v115, v115
	v_exp_f32_e32 v116, v116
	v_exp_f32_e32 v117, v117
	v_exp_f32_e32 v118, v118
	v_exp_f32_e32 v119, v119
	v_exp_f32_e32 v120, v120
	v_exp_f32_e32 v121, v121
	v_pk_add_f32 v[114:115], v[114:115], 1.0 op_sel_hi:[1,0]
	v_pk_add_f32 v[116:117], v[116:117], 1.0 op_sel_hi:[1,0]
	v_pk_add_f32 v[118:119], v[118:119], 1.0 op_sel_hi:[1,0]
	v_pk_add_f32 v[120:121], v[120:121], 1.0 op_sel_hi:[1,0]
	v_rcp_f32_e32 v114, v114
	v_rcp_f32_e32 v115, v115
	v_rcp_f32_e32 v116, v116
	v_rcp_f32_e32 v117, v117
	v_rcp_f32_e32 v118, v118
	v_rcp_f32_e32 v119, v119
	v_rcp_f32_e32 v120, v120
	v_rcp_f32_e32 v121, v121
	v_pk_mul_f32 v[98:99], v[114:115], v[98:99]
	v_pk_mul_f32 v[100:101], v[116:117], v[100:101]
	v_pk_mul_f32 v[102:103], v[118:119], v[102:103]
	v_pk_mul_f32 v[104:105], v[120:121], v[104:105]
	v_cvt_pk_fp8_f32 v130, v98, v99
	v_cvt_pk_fp8_f32 v131, v102, v103
	v_cvt_pk_fp8_f32 v130, v100, v101 op_sel:[0,0,1]
	v_cvt_pk_fp8_f32 v131, v104, v105 op_sel:[0,0,1]
	global_store_dwordx2 v202, v[130:131], s[0:1]
	v_pk_mul_f32 v[106:107], v[122:123], v[106:107]
	v_pk_mul_f32 v[108:109], v[124:125], v[108:109]
	v_pk_mul_f32 v[110:111], v[126:127], v[110:111]
	v_pk_mul_f32 v[112:113], v[128:129], v[112:113]
	v_exp_f32_e32 v122, v122
	v_exp_f32_e32 v123, v123
	v_exp_f32_e32 v124, v124
	v_exp_f32_e32 v125, v125
	v_exp_f32_e32 v126, v126
	v_exp_f32_e32 v127, v127
	v_exp_f32_e32 v128, v128
	v_exp_f32_e32 v129, v129
	v_pk_add_f32 v[122:123], v[122:123], 1.0 op_sel_hi:[1,0]
	v_pk_add_f32 v[124:125], v[124:125], 1.0 op_sel_hi:[1,0]
	v_pk_add_f32 v[126:127], v[126:127], 1.0 op_sel_hi:[1,0]
	v_pk_add_f32 v[128:129], v[128:129], 1.0 op_sel_hi:[1,0]
	v_rcp_f32_e32 v122, v122
	v_rcp_f32_e32 v123, v123
	v_rcp_f32_e32 v124, v124
	v_rcp_f32_e32 v125, v125
	v_rcp_f32_e32 v126, v126
	v_rcp_f32_e32 v127, v127
	v_rcp_f32_e32 v128, v128
	v_rcp_f32_e32 v129, v129
	v_pk_mul_f32 v[106:107], v[122:123], v[106:107]
	v_pk_mul_f32 v[108:109], v[124:125], v[108:109]
	v_pk_mul_f32 v[110:111], v[126:127], v[110:111]
	v_pk_mul_f32 v[112:113], v[128:129], v[112:113]
	v_cvt_pk_fp8_f32 v134, v106, v107
	v_cvt_pk_fp8_f32 v135, v110, v111
	v_cvt_pk_fp8_f32 v134, v108, v109 op_sel:[0,0,1]
	v_cvt_pk_fp8_f32 v135, v112, v113 op_sel:[0,0,1]
	v_add_u32_e32 v133, 0xe000, v202
	global_store_dwordx2 v133, v[134:135], s[0:1]
	v_mfma_f32_32x32x16_bf16 v[114:129], v[136:139], v[136:139], 0
	v_mfma_f32_32x32x16_bf16 v[98:113], v[136:139], v[136:139], 0
	v_pk_mul_f32 v[66:67], v[82:83], v[66:67]
	v_pk_mul_f32 v[68:69], v[84:85], v[68:69]
	v_pk_mul_f32 v[70:71], v[86:87], v[70:71]
	v_pk_mul_f32 v[72:73], v[88:89], v[72:73]
	v_exp_f32_e32 v82, v82
	v_exp_f32_e32 v83, v83
	v_exp_f32_e32 v84, v84
	v_exp_f32_e32 v85, v85
	v_exp_f32_e32 v86, v86
	v_exp_f32_e32 v87, v87
	v_exp_f32_e32 v88, v88
	v_exp_f32_e32 v89, v89
	v_pk_add_f32 v[82:83], v[82:83], 1.0 op_sel_hi:[1,0]
	v_pk_add_f32 v[84:85], v[84:85], 1.0 op_sel_hi:[1,0]
	v_pk_add_f32 v[86:87], v[86:87], 1.0 op_sel_hi:[1,0]
	v_pk_add_f32 v[88:89], v[88:89], 1.0 op_sel_hi:[1,0]
	v_rcp_f32_e32 v82, v82
	v_rcp_f32_e32 v83, v83
	v_rcp_f32_e32 v84, v84
	v_rcp_f32_e32 v85, v85
	v_rcp_f32_e32 v86, v86
	v_rcp_f32_e32 v87, v87
	v_rcp_f32_e32 v88, v88
	v_rcp_f32_e32 v89, v89
	v_pk_mul_f32 v[66:67], v[82:83], v[66:67]
	v_pk_mul_f32 v[68:69], v[84:85], v[68:69]
	v_pk_mul_f32 v[70:71], v[86:87], v[70:71]
	v_pk_mul_f32 v[72:73], v[88:89], v[72:73]
	v_cvt_pk_fp8_f32 v130, v66, v67
	v_cvt_pk_fp8_f32 v131, v70, v71
	v_cvt_pk_fp8_f32 v130, v68, v69 op_sel:[0,0,1]
	v_cvt_pk_fp8_f32 v131, v72, v73 op_sel:[0,0,1]
	v_add_u32_e32 v132, 0x1c000, v202
	global_store_dwordx2 v132, v[130:131], s[0:1]
	v_pk_mul_f32 v[74:75], v[90:91], v[74:75]
	v_pk_mul_f32 v[76:77], v[92:93], v[76:77]
	v_pk_mul_f32 v[78:79], v[94:95], v[78:79]
	v_pk_mul_f32 v[80:81], v[96:97], v[80:81]
	v_exp_f32_e32 v90, v90
	v_exp_f32_e32 v91, v91
	v_exp_f32_e32 v92, v92
	v_exp_f32_e32 v93, v93
	v_exp_f32_e32 v94, v94
	v_exp_f32_e32 v95, v95
	v_exp_f32_e32 v96, v96
	v_exp_f32_e32 v97, v97
	v_pk_add_f32 v[90:91], v[90:91], 1.0 op_sel_hi:[1,0]
	v_pk_add_f32 v[92:93], v[92:93], 1.0 op_sel_hi:[1,0]
	v_pk_add_f32 v[94:95], v[94:95], 1.0 op_sel_hi:[1,0]
	v_pk_add_f32 v[96:97], v[96:97], 1.0 op_sel_hi:[1,0]
	v_rcp_f32_e32 v90, v90
	v_rcp_f32_e32 v91, v91
	v_rcp_f32_e32 v92, v92
	v_rcp_f32_e32 v93, v93
	v_rcp_f32_e32 v94, v94
	v_rcp_f32_e32 v95, v95
	v_rcp_f32_e32 v96, v96
	v_rcp_f32_e32 v97, v97
	v_pk_mul_f32 v[74:75], v[90:91], v[74:75]
	v_pk_mul_f32 v[76:77], v[92:93], v[76:77]
	v_pk_mul_f32 v[78:79], v[94:95], v[78:79]
	v_pk_mul_f32 v[80:81], v[96:97], v[80:81]
	v_cvt_pk_fp8_f32 v134, v74, v75
	v_cvt_pk_fp8_f32 v135, v78, v79
	v_cvt_pk_fp8_f32 v134, v76, v77 op_sel:[0,0,1]
	v_cvt_pk_fp8_f32 v135, v80, v81 op_sel:[0,0,1]
	v_add_u32_e32 v133, 0x2a000, v202
	global_store_dwordx2 v133, v[134:135], s[0:1]
	v_mfma_f32_32x32x16_bf16 v[82:97], v[136:139], v[136:139], 0
	v_mfma_f32_32x32x16_bf16 v[66:81], v[136:139], v[136:139], 0
	v_pk_mul_f32 v[34:35], v[50:51], v[34:35]
	v_pk_mul_f32 v[36:37], v[52:53], v[36:37]
	v_pk_mul_f32 v[38:39], v[54:55], v[38:39]
	v_pk_mul_f32 v[40:41], v[56:57], v[40:41]
	v_exp_f32_e32 v50, v50
	v_exp_f32_e32 v51, v51
	v_exp_f32_e32 v52, v52
	v_exp_f32_e32 v53, v53
	v_exp_f32_e32 v54, v54
	v_exp_f32_e32 v55, v55
	v_exp_f32_e32 v56, v56
	v_exp_f32_e32 v57, v57
	v_pk_add_f32 v[50:51], v[50:51], 1.0 op_sel_hi:[1,0]
	v_pk_add_f32 v[52:53], v[52:53], 1.0 op_sel_hi:[1,0]
	v_pk_add_f32 v[54:55], v[54:55], 1.0 op_sel_hi:[1,0]
	v_pk_add_f32 v[56:57], v[56:57], 1.0 op_sel_hi:[1,0]
	v_rcp_f32_e32 v50, v50
	v_rcp_f32_e32 v51, v51
	v_rcp_f32_e32 v52, v52
	v_rcp_f32_e32 v53, v53
	v_rcp_f32_e32 v54, v54
	v_rcp_f32_e32 v55, v55
	v_rcp_f32_e32 v56, v56
	v_rcp_f32_e32 v57, v57
	v_pk_mul_f32 v[34:35], v[50:51], v[34:35]
	v_pk_mul_f32 v[36:37], v[52:53], v[36:37]
	v_pk_mul_f32 v[38:39], v[54:55], v[38:39]
	v_pk_mul_f32 v[40:41], v[56:57], v[40:41]
	v_cvt_pk_fp8_f32 v130, v34, v35
	v_cvt_pk_fp8_f32 v131, v38, v39
	v_cvt_pk_fp8_f32 v130, v36, v37 op_sel:[0,0,1]
	v_cvt_pk_fp8_f32 v131, v40, v41 op_sel:[0,0,1]
	v_add_u32_e32 v132, 0x70000, v202
	global_store_dwordx2 v132, v[130:131], s[0:1]
	v_pk_mul_f32 v[42:43], v[58:59], v[42:43]
	v_pk_mul_f32 v[44:45], v[60:61], v[44:45]
	v_pk_mul_f32 v[46:47], v[62:63], v[46:47]
	v_pk_mul_f32 v[48:49], v[64:65], v[48:49]
	v_exp_f32_e32 v58, v58
	v_exp_f32_e32 v59, v59
	v_exp_f32_e32 v60, v60
	v_exp_f32_e32 v61, v61
	v_exp_f32_e32 v62, v62
	v_exp_f32_e32 v63, v63
	v_exp_f32_e32 v64, v64
	v_exp_f32_e32 v65, v65
	v_pk_add_f32 v[58:59], v[58:59], 1.0 op_sel_hi:[1,0]
	v_pk_add_f32 v[60:61], v[60:61], 1.0 op_sel_hi:[1,0]
	v_pk_add_f32 v[62:63], v[62:63], 1.0 op_sel_hi:[1,0]
	v_pk_add_f32 v[64:65], v[64:65], 1.0 op_sel_hi:[1,0]
	v_rcp_f32_e32 v58, v58
	v_rcp_f32_e32 v59, v59
	v_rcp_f32_e32 v60, v60
	v_rcp_f32_e32 v61, v61
	v_rcp_f32_e32 v62, v62
	v_rcp_f32_e32 v63, v63
	v_rcp_f32_e32 v64, v64
	v_rcp_f32_e32 v65, v65
	v_pk_mul_f32 v[42:43], v[58:59], v[42:43]
	v_pk_mul_f32 v[44:45], v[60:61], v[44:45]
	v_pk_mul_f32 v[46:47], v[62:63], v[46:47]
	v_pk_mul_f32 v[48:49], v[64:65], v[48:49]
	v_cvt_pk_fp8_f32 v134, v42, v43
	v_cvt_pk_fp8_f32 v135, v46, v47
	v_cvt_pk_fp8_f32 v134, v44, v45 op_sel:[0,0,1]
	v_cvt_pk_fp8_f32 v135, v48, v49 op_sel:[0,0,1]
	v_add_u32_e32 v133, 0x7e000, v202
	global_store_dwordx2 v133, v[134:135], s[0:1]
	v_mfma_f32_32x32x16_bf16 v[50:65], v[136:139], v[136:139], 0
	v_mfma_f32_32x32x16_bf16 v[34:49], v[136:139], v[136:139], 0
	v_pk_mul_f32 v[2:3], v[18:19], v[2:3]
	v_pk_mul_f32 v[4:5], v[20:21], v[4:5]
	v_pk_mul_f32 v[6:7], v[22:23], v[6:7]
	v_pk_mul_f32 v[8:9], v[24:25], v[8:9]
	v_exp_f32_e32 v18, v18
	v_exp_f32_e32 v19, v19
	v_exp_f32_e32 v20, v20
	v_exp_f32_e32 v21, v21
	v_exp_f32_e32 v22, v22
	v_exp_f32_e32 v23, v23
	v_exp_f32_e32 v24, v24
	v_exp_f32_e32 v25, v25
	v_pk_add_f32 v[18:19], v[18:19], 1.0 op_sel_hi:[1,0]
	v_pk_add_f32 v[20:21], v[20:21], 1.0 op_sel_hi:[1,0]
	v_pk_add_f32 v[22:23], v[22:23], 1.0 op_sel_hi:[1,0]
	v_pk_add_f32 v[24:25], v[24:25], 1.0 op_sel_hi:[1,0]
	v_rcp_f32_e32 v18, v18
	v_rcp_f32_e32 v19, v19
	v_rcp_f32_e32 v20, v20
	v_rcp_f32_e32 v21, v21
	v_rcp_f32_e32 v22, v22
	v_rcp_f32_e32 v23, v23
	v_rcp_f32_e32 v24, v24
	v_rcp_f32_e32 v25, v25
	v_pk_mul_f32 v[2:3], v[18:19], v[2:3]
	v_pk_mul_f32 v[4:5], v[20:21], v[4:5]
	v_pk_mul_f32 v[6:7], v[22:23], v[6:7]
	v_pk_mul_f32 v[8:9], v[24:25], v[8:9]
	v_cvt_pk_fp8_f32 v130, v2, v3
	v_cvt_pk_fp8_f32 v131, v6, v7
	v_cvt_pk_fp8_f32 v130, v4, v5 op_sel:[0,0,1]
	v_cvt_pk_fp8_f32 v131, v8, v9 op_sel:[0,0,1]
	v_add_u32_e32 v132, 0x8c000, v202
	global_store_dwordx2 v132, v[130:131], s[0:1]
	v_pk_mul_f32 v[10:11], v[26:27], v[10:11]
	v_pk_mul_f32 v[12:13], v[28:29], v[12:13]
	v_pk_mul_f32 v[14:15], v[30:31], v[14:15]
	v_pk_mul_f32 v[16:17], v[32:33], v[16:17]
	v_exp_f32_e32 v26, v26
	v_exp_f32_e32 v27, v27
	v_exp_f32_e32 v28, v28
	v_exp_f32_e32 v29, v29
	v_exp_f32_e32 v30, v30
	v_exp_f32_e32 v31, v31
	v_exp_f32_e32 v32, v32
	v_exp_f32_e32 v33, v33
	v_pk_add_f32 v[26:27], v[26:27], 1.0 op_sel_hi:[1,0]
	v_pk_add_f32 v[28:29], v[28:29], 1.0 op_sel_hi:[1,0]
	v_pk_add_f32 v[30:31], v[30:31], 1.0 op_sel_hi:[1,0]
	v_pk_add_f32 v[32:33], v[32:33], 1.0 op_sel_hi:[1,0]
	v_rcp_f32_e32 v26, v26
	v_rcp_f32_e32 v27, v27
	v_rcp_f32_e32 v28, v28
	v_rcp_f32_e32 v29, v29
	v_rcp_f32_e32 v30, v30
	v_rcp_f32_e32 v31, v31
	v_rcp_f32_e32 v32, v32
	v_rcp_f32_e32 v33, v33
	v_pk_mul_f32 v[10:11], v[26:27], v[10:11]
	v_pk_mul_f32 v[12:13], v[28:29], v[12:13]
	v_pk_mul_f32 v[14:15], v[30:31], v[14:15]
	v_pk_mul_f32 v[16:17], v[32:33], v[16:17]
	v_cvt_pk_fp8_f32 v134, v10, v11
	v_cvt_pk_fp8_f32 v135, v14, v15
	v_cvt_pk_fp8_f32 v134, v12, v13 op_sel:[0,0,1]
	v_cvt_pk_fp8_f32 v135, v16, v17 op_sel:[0,0,1]
	v_add_u32_e32 v133, 0x9a000, v202
	global_store_dwordx2 v133, v[134:135], s[0:1]
	v_mfma_f32_32x32x16_bf16 v[18:33], v[136:139], v[136:139], 0
	v_mfma_f32_32x32x16_bf16 v[2:17], v[136:139], v[136:139], 0
	s_and_b64 vcc, exec, s[2:3]
	s_mov_b64 s[2:3], -1
	s_cbranch_vccnz .LBB0_1719
	s_andn2_b64 vcc, exec, s[8:9]
	s_cbranch_vccnz .LBB0_1718
	s_barrier
	s_branch .LBB0_1718
